# GU L1: K-loop start rotated per unit by (pm + 4*(pn&1)) K-pairs so that workgroups sharing a weight tile are not in lockstep (L2 reuse instead of simultaneous misses)
# speedup vs baseline: 1.0180x; 1.0180x over previous
;     __device__ bool next(int i, Unit& u) const { return map((long)i * G + c, u); }
;     ...
;     const size_t tstep = 2 * hstep;
;     const unsigned ldsw = (unsigned)wid * 1024u;
;     const int aoff = lds_byte(wr * 64 + fr, fq * 8), boff = lds_byte(wc * 32 + fr, fq * 8);
;     ...
;     Unit cur, nxt; int ui = 0;
;     if (!S.next(0, cur)) return;
;     if constexpr (GATHER) {
;         for (int k = tid >> 8;; k += 2) { Unit u; if (!S.next(k, u)) break; idxl[k * 256 + (tid & 255)] = g.ridx[(size_t)u.z * g.ridxStrideZ + u.pm * BM + (tid & 255)]; }
;         __syncthreads();
; #pragma unroll
;         for (int hh = 0; hh < 2; ++hh)
; #pragma unroll
;             for (int i = 0; i < 2; ++i) voffA[hh][i] = (unsigned)idxl[hh * HALF + sR[i]] * (unsigned)(K * 2) + (unsigned)sC[i] * 2u;
;     } else {
; #pragma unroll
;         for (int hh = 0; hh < 2; ++hh)
; #pragma unroll
;             for (int i = 0; i < 2; ++i) voffA[hh][i] = (TILED & 1) ? (unsigned)hh * (unsigned)(HALF * K * 2) + (unsigned)(sR[i] * BK + sC[i]) * 2u : (unsigned)((hh * HALF + sR[i]) * K + sC[i]) * 2u;
;     }
; #pragma unroll
;     for (int hh = 0; hh < 2; ++hh)
; #pragma unroll
;         for (int i = 0; i < 2; ++i) voffN[hh][i] = voffA[hh][i];
;     f32x4 acc[2][2][4][2];
; #pragma unroll
;     for (int a = 0; a < 2; ++a)
; #pragma unroll
;         for (int b = 0; b < 2; ++b)
; #pragma unroll
;             for (int m = 0; m < 4; ++m)
; #pragma unroll
;                 for (int n = 0; n < 2; ++n) acc[a][b][m][n] = (f32x4){0.f, 0.f, 0.f, 0.f};
;     bf16x8 At[4][2], B0[2][2], B1[2][2];
;     auto k0t = [&](const Unit& u) -> size_t { return (SPLITK && u.kq >= 0) ? (size_t)(12 * u.kq - (u.kq == 3 ? 2 : 0)) : (size_t)0; };
;     const char* cA = (const char*)(g.A + (size_t)cur.z * g.aStrideZ) + (GATHER ? (size_t)0 : (size_t)cur.pm * tstep) + k0t(cur) * kstepA;
;     const char* cB = (const char*)(g.Bt + (size_t)cur.z * g.bStrideZ) + (size_t)cur.pn * tstep + k0t(cur) * kstepB;
;     PG8_STAGE(PG8_SB(0, 0), cB, voffB); PG8_STAGE(PG8_SB(0, 1), cB + hstep, voffB); PG8_STAGE(PG8_SA(0, 0), cA, voffA[0]); PG8_STAGE(PG8_SA(0, 1), cA, voffA[1]);
;     if (wr == 1) PG8_BAR;
;     PG8_WAIT_V(2); PG8_BAR;
;     PG8_STAGE(PG8_SB(1, 0), cB + kstepB, voffB); PG8_STAGE(PG8_SA(1, 0), cA + kstepA, voffA[0]); PG8_STAGE(PG8_SB(1, 1), cB + hstep + kstepB, voffB);
;     PG8_WAIT_V(6); PG8_BAR;
.LBB0_2329:
	s_lshl_b32 s7, s7, 3
	s_lshl_b32 s39, s6, 6
	s_lshl_b32 s6, s0, 5
	s_sub_i32 s1, s1, s7
	s_and_b32 s40, s6, 0x60
	s_add_u32 s6, s2, 0x4000
	s_addc_u32 s7, s3, 0
	s_add_i32 m0, s17, 0x18000
	v_lshl_add_u64 v[4:5], s[6:7], 0, v[132:133]
	s_waitcnt vmcnt(2)
	s_barrier
	global_load_lds_dwordx4 v[4:5], off
	s_add_i32 m0, s17, 0x1a000
	v_lshl_add_u64 v[4:5], s[6:7], 0, v[134:135]
	s_add_u32 s6, s90, 0x4213680
	s_addc_u32 s7, s91, 0
	s_add_i32 s41, s17, 0x8000
	s_add_i32 s42, s17, 0xa000
	global_load_lds_dwordx4 v[4:5], off
	v_lshl_add_u64 v[4:5], s[6:7], 0, v[136:137]
	s_mov_b32 m0, s41
	s_add_u32 s10, s2, 0x44000
	global_load_lds_dwordx4 v[4:5], off
	v_lshl_add_u64 v[2:3], s[6:7], 0, v[2:3]
	s_mov_b32 m0, s42
	s_addc_u32 s11, s3, 0
	global_load_lds_dwordx4 v[2:3], off
	s_add_i32 m0, s17, 0x1c000
	v_lshl_add_u64 v[2:3], s[10:11], 0, v[132:133]
	global_load_lds_dwordx4 v[2:3], off
	v_lshl_add_u64 v[2:3], s[10:11], 0, v[134:135]
	s_add_i32 m0, s17, 0x1e000
	v_bfe_u32 v4, v6, 4, 2
	global_load_lds_dwordx4 v[2:3], off
	v_lshrrev_b32_e32 v2, 4, v6
	v_and_b32_e32 v3, 15, v6
	v_and_b32_e32 v6, 7, v6
	v_bitop3_b32 v2, v2, v6, 3 bitop3:0x6c
	s_cmpk_lt_u32 s8, 0x100
	v_lshlrev_b32_e32 v7, 4, v2
	v_or_b32_e32 v2, s40, v3
	s_cselect_b64 s[8:9], -1, 0
	s_lshl_b32 s0, s0, 6
	v_or_b32_e32 v5, s39, v3
	v_lshlrev_b32_e32 v9, 7, v2
	v_and_or_b32 v2, s39, 64, v3
	s_and_b32 s0, s0, 64
	s_sext_i32_i8 s52, s1
	v_lshlrev_b32_e32 v5, 7, v5
	s_waitcnt vmcnt(6)
	v_lshl_or_b32 v136, v4, 4, s0
	v_readlane_b32 s0, v250, 32
	v_lshlrev_b32_e32 v2, 6, v2
	v_or_b32_e32 v8, v5, v7
	v_readlane_b32 s1, v250, 33
	v_or_b32_e32 v4, 0x800, v2
	v_or_b32_e32 v6, 0xc00, v2
	v_bitop3_b32 v3, v5, 64, v7 bitop3:0x36
	v_or_b32_e32 v159, v9, v7
	v_lshl_add_u64 v[138:139], s[0:1], 0, v[136:137]
	v_bitop3_b32 v160, v9, 64, v7 bitop3:0x36
	s_add_i32 s43, 0, 0x10000
	s_add_i32 s44, 0, 0x10800
	s_add_i32 s45, 0, 0x14000
	s_add_i32 s46, 0, 0x14800
	v_add_u32_e32 v161, 0, v8
	v_add_u32_e32 v162, 0, v3
	s_add_i32 s47, 0, 0x18800
	s_add_i32 s48, 0, 0x1c800
	s_mov_b64 s[10:11], 0x80
	v_lshlrev_b32_e32 v140, 1, v2
	v_lshlrev_b32_e32 v142, 1, v4
	v_lshlrev_b32_e32 v144, 1, v6
	v_mov_b32_e32 v163, 0xc60000
	s_barrier
	s_mov_b32 s99, 0
	s_branch .LBB0_2332

;     __device__ bool next(int i, Unit& u) const { return map((long)i * G + c, u); }
;     __device__ bool next(int i, Unit& u) const { if (!p.next(i, u)) return false; if (u.pn >= 4) u.pn += 2; return true; }
;     __device__ bool next(int i, Unit& u) const { const int L = i * G + c; if (L >= 4 * 66) return false; const int wi = L / 66; u.kq = -1; u.z = 0; u.pm = wi < 2 ? 4 + wi : 6 + wi; u.pn = L % 66; return true; }
;     __device__ bool next(int i, Unit& u) const { if (!p.next(i, u)) return false; if (u.pn >= 4) u.pn += 12; return true; }
;     __device__ bool next(int i, Unit& u) const { const int L = i * G + c; if (L >= total) return false; u.kq = -1; u.z = 0; u.pm = wt0 + L / nTok; u.pn = tok0 + L % nTok; return true; }
;     __device__ bool next(int i, Unit& u) const { if (i > 0 || c >= 48) return false; const int t = c >> 1; u.kq = c & 1; u.z = 0; u.pm = 4 + (t >> 1); u.pn = 64 + (t & 1); return true; }
;     __device__ bool next(int i, Unit& u) const {
;         const int x = c & 7, j = (c >> 3) + i * (G >> 3), per = nM * nN;
;         if (j >= 2 * per) return false;
;         const int el = j / per, rem = j % per, grp = rem / (nM * GP), w = rem % (nM * GP);
;         u.kq = -1; u.z = 2 * x + el; u.pm = w % nM; u.pn = grp * GP + w / nM; return true;
;     ...
;         const bool has_next = S.next(ui + 1, nxt);
;         const char* nA = has_next ? (const char*)(g.A + (size_t)nxt.z * g.aStrideZ) + (GATHER ? (size_t)0 : (size_t)nxt.pm * tstep) + k0t(nxt) * kstepA : cA;
;         const char* nB = has_next ? (const char*)(g.Bt + (size_t)nxt.z * g.bStrideZ) + (size_t)nxt.pn * tstep + k0t(nxt) * kstepB : cB;
.LBB0_2331:
	s_mov_b32 s99, s100
	s_andn2_b64 vcc, exec, s[0:1]
	v_mov_b32_e32 v148, v164
	v_mov_b32_e32 v150, v165
	s_mov_b32 s51, s49
	s_mov_b32 s52, s50
	s_mov_b32 s16, s12
	s_mov_b64 s[2:3], s[14:15]
	v_mov_b64_e32 v[152:153], v[146:147]
	s_cbranch_vccz .LBB0_2345
.LBB0_2332:
	s_add_i32 s38, s38, 1
	s_mul_i32 s0, s38, s29
	s_add_i32 s0, s0, s75
	s_cmpk_lt_i32 s0, 0x160
	s_cselect_b64 s[18:19], -1, 0
	s_cmpk_gt_i32 s0, 0x15f
	s_cbranch_scc1 .LBB0_2334
	s_mul_hi_i32 s1, s0, 0x2e8ba2e9
	s_lshr_b32 s12, s1, 31
	s_ashr_i32 s1, s1, 5
	s_add_i32 s1, s1, s12
	s_mul_i32 s12, s1, 0xb0
	s_sub_i32 s0, s0, s12
	s_lshr_b32 s12, s0, 27
	s_and_b32 s12, s12, 15
	s_add_i32 s12, s0, s12
	s_sext_i32_i16 s13, s12
	s_and_b32 s12, s12, 0xfff0
	s_sub_i32 s0, s0, s12
	s_add_i32 s49, s1, s28
	s_bfe_i32 s1, s0, 0x80000
	s_bfe_u32 s1, s1, 0x3000c
	s_add_i32 s1, s0, s1
	s_bfe_i32 s12, s1, 0x80000
	s_and_b32 s1, s1, 0xf8
	s_ashr_i32 s13, s13, 4
	s_sext_i32_i16 s12, s12
	s_sub_i32 s0, s0, s1
	s_sext_i32_i8 s50, s0
	s_lshl_b32 s0, s13, 1
	s_ashr_i32 s1, s12, 3
	s_add_i32 s12, s0, s1
	s_and_b32 s101, s12, 1
	s_lshl_b32 s101, s101, 2
	s_add_i32 s101, s101, s50
	s_and_b32 s101, s101, 7
	s_lshl_b32 s100, s101, 8

; #define PG8_STAGE(bufoff, gbase, voff) do { _Pragma("unroll") for (int _i = 0; _i < 2; ++_i) \
;         __builtin_amdgcn_global_load_lds((const unsigned*)((const char*)(gbase) + (voff)[_i]), (LAS unsigned*)(lds + (bufoff) + ldsw + _i * 8192), 16, 0, 0); } while (0)
; #define PG8_LDA(dst, b, h) do { _Pragma("unroll") for (int m = 0; m < 4; ++m) _Pragma("unroll") for (int k = 0; k < 2; ++k) dst[m][k] = *(const LAS bf16x8*)(lds + PG8_SA(b, h) + ((aoff ^ (k * 64)) + m * 2048)); } while (0)
; #define PG8_LDB(dst, b, h) do { _Pragma("unroll") for (int n = 0; n < 2; ++n) _Pragma("unroll") for (int k = 0; k < 2; ++k) dst[n][k] = *(const LAS bf16x8*)(lds + PG8_SB(b, h) + ((boff ^ (k * 64)) + n * 2048)); } while (0)
; #define PG8_BAR __builtin_amdgcn_s_barrier()
;     ...
;             const bool last = (t == nt - 2);
;             const char* a1 = cA + (size_t)(t + 1) * kstepA;
;             const char* a2 = last ? nA : cA + (size_t)(t + 2) * kstepA; const char* b2 = last ? nB : cB + (size_t)(t + 2) * kstepB;
;             const char* a3 = a2 + kstepA; const char* b3 = b2 + kstepB;
;             unsigned vs[2][2];
;             if constexpr (GATHER) {
;                 if (last && has_next) {
; #pragma unroll
;                     for (int hh = 0; hh < 2; ++hh)
; #pragma unroll
;                         for (int i = 0; i < 2; ++i) voffN[hh][i] = (unsigned)idxl[(ui + 1) * 256 + hh * HALF + sR[i]] * (unsigned)(K * 2) + (unsigned)sC[i] * 2u;
;                 }
; #pragma unroll
;                 for (int hh = 0; hh < 2; ++hh)
; #pragma unroll
;                     for (int i = 0; i < 2; ++i) vs[hh][i] = last ? voffN[hh][i] : voffA[hh][i];
;             } else {
; #pragma unroll
;                 for (int hh = 0; hh < 2; ++hh)
; #pragma unroll
;                     for (int i = 0; i < 2; ++i) vs[hh][i] = voffA[hh][i];
;             }
;             PG8_LDB(B0, 0, 0); PG8_LDB(B1, 0, 1); PG8_SCHED; PG8_LDA(At, 0, 0); PG8_STAGE(PG8_SA(1, 1), a1, voffA[1]);
;             PG8_WAIT_V(8); PG8_WAIT_L(0); PG8_BAR; if (do0) { PG8_MMA(0, 0, At, B0); PG8_MMA(0, 1, At, B1); } PG8_BAR; PG8_SCHED;
;     ...
;         for (int a = 0; a < 2; ++a)
; #pragma unroll
;             for (int b = 0; b < 2; ++b)
; #pragma unroll
;                 for (int m = 0; m < 4; ++m)
; #pragma unroll
;                     for (int n = 0; n < 2; ++n) acc[a][b][m][n] = (f32x4){0.f, 0.f, 0.f, 0.f};
.LBB0_2336:
	s_lshl_b32 s13, s38, 10
	s_add_i32 s13, s13, 0
	s_add_i32 s13, s13, 0x20000
	v_lshl_add_u32 v141, v131, 2, s13
	v_lshl_add_u32 v143, v158, 2, s13
	v_mov_b32_e32 v149, v137
	v_mov_b32_e32 v151, v137
	s_add_u32 s101, s99, 0x100
	s_and_b32 s101, s101, 0x7ff
	s_lshl_b32 s101, s101, 7
	s_add_u32 s13, s2, s101
	s_addc_u32 s53, s3, 0
	s_mov_b32 s20, s99
	s_mov_b32 s21, 0
	v_mov_b32_e32 v2, 0
	v_lshl_add_u64 v[154:155], s[6:7], 0, v[150:151]
	v_lshl_add_u64 v[156:157], s[6:7], 0, v[148:149]
	s_mov_b32 s54, -2
	v_mov_b32_e32 v164, v148
	v_mov_b32_e32 v165, v150
	v_mov_b64_e32 v[146:147], v[152:153]
	v_mov_b32_e32 v3, v2
	v_mov_b32_e32 v4, v2
	v_mov_b32_e32 v5, v2
	v_mov_b32_e32 v6, v2
	v_mov_b32_e32 v7, v2
	v_mov_b32_e32 v8, v2
	v_mov_b32_e32 v9, v2
	v_mov_b32_e32 v18, v2
	v_mov_b32_e32 v19, v2
	v_mov_b32_e32 v20, v2
	v_mov_b32_e32 v21, v2
	v_mov_b32_e32 v22, v2
	v_mov_b32_e32 v23, v2
	v_mov_b32_e32 v24, v2
	v_mov_b32_e32 v25, v2
	v_mov_b32_e32 v34, v2
	v_mov_b32_e32 v35, v2
	v_mov_b32_e32 v36, v2
	v_mov_b32_e32 v37, v2
	v_mov_b32_e32 v38, v2
	v_mov_b32_e32 v39, v2
	v_mov_b32_e32 v40, v2
	v_mov_b32_e32 v41, v2
	v_mov_b32_e32 v50, v2
	v_mov_b32_e32 v51, v2
	v_mov_b32_e32 v52, v2
	v_mov_b32_e32 v53, v2
	v_mov_b32_e32 v54, v2
	v_mov_b32_e32 v55, v2
	v_mov_b32_e32 v56, v2
	v_mov_b32_e32 v57, v2
	v_mov_b32_e32 v10, v2
	v_mov_b32_e32 v11, v2
	v_mov_b32_e32 v12, v2
	v_mov_b32_e32 v13, v2
	v_mov_b32_e32 v14, v2
	v_mov_b32_e32 v15, v2
	v_mov_b32_e32 v16, v2
	v_mov_b32_e32 v17, v2
	v_mov_b32_e32 v26, v2
	v_mov_b32_e32 v27, v2
	v_mov_b32_e32 v28, v2
	v_mov_b32_e32 v29, v2
	v_mov_b32_e32 v30, v2
	v_mov_b32_e32 v31, v2
	v_mov_b32_e32 v32, v2
	v_mov_b32_e32 v33, v2
	v_mov_b32_e32 v42, v2
	v_mov_b32_e32 v43, v2
	v_mov_b32_e32 v44, v2
	v_mov_b32_e32 v45, v2
	v_mov_b32_e32 v46, v2
	v_mov_b32_e32 v47, v2
	v_mov_b32_e32 v48, v2
	v_mov_b32_e32 v49, v2
	v_mov_b32_e32 v58, v2
	v_mov_b32_e32 v59, v2
	v_mov_b32_e32 v60, v2
	v_mov_b32_e32 v61, v2
	v_mov_b32_e32 v62, v2
	v_mov_b32_e32 v63, v2
	v_mov_b32_e32 v64, v2
	v_mov_b32_e32 v65, v2
	v_mov_b32_e32 v66, v2
	v_mov_b32_e32 v67, v2
	v_mov_b32_e32 v68, v2
	v_mov_b32_e32 v69, v2
	v_mov_b32_e32 v70, v2
	v_mov_b32_e32 v71, v2
	v_mov_b32_e32 v72, v2
	v_mov_b32_e32 v73, v2
	v_mov_b32_e32 v82, v2
	v_mov_b32_e32 v83, v2
	v_mov_b32_e32 v84, v2
	v_mov_b32_e32 v85, v2
	v_mov_b32_e32 v86, v2
	v_mov_b32_e32 v87, v2
	v_mov_b32_e32 v88, v2
	v_mov_b32_e32 v89, v2
	v_mov_b32_e32 v98, v2
	v_mov_b32_e32 v99, v2
	v_mov_b32_e32 v100, v2
	v_mov_b32_e32 v101, v2
	v_mov_b32_e32 v102, v2
	v_mov_b32_e32 v103, v2
	v_mov_b32_e32 v104, v2
	v_mov_b32_e32 v105, v2
	v_mov_b32_e32 v114, v2
	v_mov_b32_e32 v115, v2
	v_mov_b32_e32 v116, v2
	v_mov_b32_e32 v117, v2
	v_mov_b32_e32 v118, v2
	v_mov_b32_e32 v119, v2
	v_mov_b32_e32 v120, v2
	v_mov_b32_e32 v121, v2
	v_mov_b32_e32 v74, v2
	v_mov_b32_e32 v75, v2
	v_mov_b32_e32 v76, v2
	v_mov_b32_e32 v77, v2
	v_mov_b32_e32 v78, v2
	v_mov_b32_e32 v79, v2
	v_mov_b32_e32 v80, v2
	v_mov_b32_e32 v81, v2
	v_mov_b32_e32 v90, v2
	v_mov_b32_e32 v91, v2
	v_mov_b32_e32 v92, v2
	v_mov_b32_e32 v93, v2
	v_mov_b32_e32 v94, v2
	v_mov_b32_e32 v95, v2
	v_mov_b32_e32 v96, v2
	v_mov_b32_e32 v97, v2
	v_mov_b32_e32 v106, v2
	v_mov_b32_e32 v107, v2
	v_mov_b32_e32 v108, v2
	v_mov_b32_e32 v109, v2
	v_mov_b32_e32 v110, v2
	v_mov_b32_e32 v111, v2
	v_mov_b32_e32 v112, v2
	v_mov_b32_e32 v113, v2
	v_mov_b32_e32 v122, v2
	v_mov_b32_e32 v123, v2
	v_mov_b32_e32 v124, v2
	v_mov_b32_e32 v125, v2
	v_mov_b32_e32 v126, v2
	v_mov_b32_e32 v127, v2
	v_mov_b32_e32 v128, v2
	v_mov_b32_e32 v129, v2
	s_branch .LBB0_2338
.LBB0_2337:
	v_add_u32_e32 v136, s43, v159
	v_add_u32_e32 v145, s43, v160
	ds_read_b128 v[166:169], v136
	ds_read_b128 v[170:173], v145
	v_add_u32_e32 v136, s44, v159
	v_add_u32_e32 v145, s44, v160
	ds_read_b128 v[174:177], v136
	ds_read_b128 v[178:181], v145
	v_add_u32_e32 v136, s45, v159
	v_add_u32_e32 v145, s45, v160
	ds_read_b128 v[182:185], v136
	ds_read_b128 v[186:189], v145
	v_add_u32_e32 v136, s46, v159
	v_add_u32_e32 v145, s46, v160
	ds_read_b128 v[190:193], v136
	ds_read_b128 v[194:197], v145
	s_add_u32 s101, s20, 0x100
	s_and_b32 s101, s101, 0x7ff
	s_and_b64 s[22:23], s[2:3], exec
	s_cselect_b32 s101, s100, s101
	s_cselect_b32 s22, s14, s13
	s_cselect_b32 s23, s15, s53
	s_cselect_b32 s24, s100, 0
	s_lshl_b32 s24, s24, 7
	s_add_u32 s22, s22, s24
	s_addc_u32 s23, s23, 0
	s_add_u32 s26, s82, s101
	s_addc_u32 s27, s83, 0
	s_add_u32 s24, s22, 0x4000
	s_addc_u32 s25, s23, 0
	v_cndmask_b32_e64 v136, v152, v146, s[2:3]
	v_cndmask_b32_e64 v232, v153, v147, s[2:3]
	v_cndmask_b32_e64 v145, v148, v164, s[2:3]
	v_cndmask_b32_e64 v149, v150, v165, s[2:3]
	v_lshl_add_u64 v[234:235], v[156:157], 0, s[20:21]
	s_add_i32 m0, s17, 0xc000
	ds_read_b128 v[200:203], v161
	ds_read_b128 v[204:207], v161 offset:2048
	ds_read_b128 v[208:211], v162
	ds_read_b128 v[212:215], v162 offset:2048
	ds_read_b128 v[216:219], v161 offset:4096
	ds_read_b128 v[220:223], v161 offset:6144
	ds_read_b128 v[224:227], v162 offset:4096
	ds_read_b128 v[228:231], v162 offset:6144
	global_load_lds_dwordx4 v[234:235], off
	v_lshl_add_u64 v[234:235], v[154:155], 0, s[20:21]
	s_add_i32 m0, s17, 0xe000
	s_nop 0
	global_load_lds_dwordx4 v[234:235], off
	s_waitcnt vmcnt(8)
	s_waitcnt lgkmcnt(0)
	s_barrier
; #define PG8_STAGE(bufoff, gbase, voff) do { _Pragma("unroll") for (int _i = 0; _i < 2; ++_i) \
;         __builtin_amdgcn_global_load_lds((const unsigned*)((const char*)(gbase) + (voff)[_i]), (LAS unsigned*)(lds + (bufoff) + ldsw + _i * 8192), 16, 0, 0); } while (0)
; #define PG8_LDA(dst, b, h) do { _Pragma("unroll") for (int m = 0; m < 4; ++m) _Pragma("unroll") for (int k = 0; k < 2; ++k) dst[m][k] = *(const LAS bf16x8*)(lds + PG8_SA(b, h) + ((aoff ^ (k * 64)) + m * 2048)); } while (0)
; #define PG8_LDB(dst, b, h) do { _Pragma("unroll") for (int n = 0; n < 2; ++n) _Pragma("unroll") for (int k = 0; k < 2; ++k) dst[n][k] = *(const LAS bf16x8*)(lds + PG8_SB(b, h) + ((boff ^ (k * 64)) + n * 2048)); } while (0)
; #define PG8_MMA(ai, bj, At, Bt) do { __builtin_amdgcn_s_setprio(1); _Pragma("unroll") for (int m = 0; m < 4; ++m) _Pragma("unroll") for (int n = 0; n < 2; ++n) _Pragma("unroll") for (int k = 0; k < 2; ++k) \
;         acc[ai][bj][m][n] = __builtin_amdgcn_mfma_f32_16x16x32_bf16(Bt[n][k], At[m][k], acc[ai][bj][m][n], 0, 0, 0); __builtin_amdgcn_s_setprio(0); } while (0)
; #define PG8_WAIT_V(n) asm volatile("s_waitcnt vmcnt(" #n ")" ::: "memory")
; #define PG8_WAIT_L(n) asm volatile("s_waitcnt lgkmcnt(" #n ")" ::: "memory")
; #define PG8_BAR __builtin_amdgcn_s_barrier()
; #define PG8_SCHED __builtin_amdgcn_sched_barrier(0)
;     ...
;             PG8_WAIT_V(8); PG8_WAIT_L(0); PG8_BAR; if (do0) { PG8_MMA(0, 0, At, B0); PG8_MMA(0, 1, At, B1); } PG8_BAR; PG8_SCHED;
;             PG8_LDA(At, 0, 1); PG8_STAGE(PG8_SB(0, 0), b2, voffB); PG8_STAGE(PG8_SB(0, 1), b2 + hstep, voffB); PG8_STAGE(PG8_SA(0, 0), a2, vs[0]);
;             PG8_WAIT_V(8); PG8_WAIT_L(0); PG8_BAR; if (do1) { PG8_MMA(1, 0, At, B0); PG8_MMA(1, 1, At, B1); } PG8_BAR; PG8_SCHED;
;             PG8_LDB(B0, 1, 0); PG8_LDB(B1, 1, 1); PG8_SCHED; PG8_LDA(At, 1, 0); PG8_STAGE(PG8_SA(0, 1), a2, vs[1]);
;             PG8_WAIT_V(8); PG8_WAIT_L(0); PG8_BAR; if (do0) { PG8_MMA(0, 0, At, B0); PG8_MMA(0, 1, At, B1); } PG8_BAR; PG8_SCHED;
	s_setprio 1
	s_waitcnt lgkmcnt(0)
	v_mfma_f32_16x16x32_bf16 v[126:129], v[166:169], v[200:203], v[126:129]
	v_mfma_f32_16x16x32_bf16 v[122:125], v[174:177], v[200:203], v[122:125]
	v_mfma_f32_16x16x32_bf16 v[110:113], v[166:169], v[204:207], v[110:113]
	v_mfma_f32_16x16x32_bf16 v[106:109], v[174:177], v[204:207], v[106:109]
	v_mfma_f32_16x16x32_bf16 v[94:97], v[166:169], v[216:219], v[94:97]
	v_mfma_f32_16x16x32_bf16 v[90:93], v[174:177], v[216:219], v[90:93]
	v_mfma_f32_16x16x32_bf16 v[78:81], v[166:169], v[220:223], v[78:81]
	v_mfma_f32_16x16x32_bf16 v[74:77], v[174:177], v[220:223], v[74:77]
	v_mfma_f32_16x16x32_bf16 v[126:129], v[170:173], v[208:211], v[126:129]
	v_mfma_f32_16x16x32_bf16 v[122:125], v[178:181], v[208:211], v[122:125]
	v_mfma_f32_16x16x32_bf16 v[110:113], v[170:173], v[212:215], v[110:113]
	v_mfma_f32_16x16x32_bf16 v[106:109], v[178:181], v[212:215], v[106:109]
	v_mfma_f32_16x16x32_bf16 v[94:97], v[170:173], v[224:227], v[94:97]
	v_mfma_f32_16x16x32_bf16 v[90:93], v[178:181], v[224:227], v[90:93]
	v_mfma_f32_16x16x32_bf16 v[78:81], v[170:173], v[228:231], v[78:81]
	v_mfma_f32_16x16x32_bf16 v[74:77], v[178:181], v[228:231], v[74:77]
	s_setprio 0
	s_setprio 1
	v_mfma_f32_16x16x32_bf16 v[118:121], v[182:185], v[200:203], v[118:121]
	v_mfma_f32_16x16x32_bf16 v[114:117], v[190:193], v[200:203], v[114:117]
	v_mfma_f32_16x16x32_bf16 v[102:105], v[182:185], v[204:207], v[102:105]
	v_mfma_f32_16x16x32_bf16 v[98:101], v[190:193], v[204:207], v[98:101]
	v_mfma_f32_16x16x32_bf16 v[86:89], v[182:185], v[216:219], v[86:89]
	v_mfma_f32_16x16x32_bf16 v[82:85], v[190:193], v[216:219], v[82:85]
	v_mfma_f32_16x16x32_bf16 v[70:73], v[182:185], v[220:223], v[70:73]
	v_mfma_f32_16x16x32_bf16 v[66:69], v[190:193], v[220:223], v[66:69]
	v_mfma_f32_16x16x32_bf16 v[118:121], v[186:189], v[208:211], v[118:121]
	v_mfma_f32_16x16x32_bf16 v[114:117], v[194:197], v[208:211], v[114:117]
	v_mfma_f32_16x16x32_bf16 v[102:105], v[186:189], v[212:215], v[102:105]
	v_mfma_f32_16x16x32_bf16 v[98:101], v[194:197], v[212:215], v[98:101]
	v_mfma_f32_16x16x32_bf16 v[86:89], v[186:189], v[224:227], v[86:89]
	v_mfma_f32_16x16x32_bf16 v[82:85], v[194:197], v[224:227], v[82:85]
	v_mfma_f32_16x16x32_bf16 v[70:73], v[186:189], v[228:231], v[70:73]
	v_mfma_f32_16x16x32_bf16 v[66:69], v[194:197], v[228:231], v[66:69]
	s_setprio 0
	s_barrier
	s_add_i32 s2, s43, s34
	v_lshl_add_u64 v[234:235], s[22:23], 0, v[132:133]
	s_mov_b32 m0, s2
	ds_read_b128 v[200:203], v161 offset:16384
	ds_read_b128 v[204:207], v161 offset:18432
	ds_read_b128 v[208:211], v162 offset:16384
	ds_read_b128 v[212:215], v162 offset:18432
	ds_read_b128 v[216:219], v161 offset:20480
	ds_read_b128 v[220:223], v161 offset:22528
	ds_read_b128 v[224:227], v162 offset:20480
	ds_read_b128 v[228:231], v162 offset:22528
	global_load_lds_dwordx4 v[234:235], off
	s_add_i32 m0, s2, 0x2000
	s_add_u32 s2, s22, 0x40000
	v_lshl_add_u64 v[234:235], s[22:23], 0, v[134:135]
	s_addc_u32 s3, s23, 0
	s_add_i32 s55, s45, s34
	global_load_lds_dwordx4 v[234:235], off
	v_lshl_add_u64 v[234:235], s[2:3], 0, v[132:133]
	s_mov_b32 m0, s55
	v_mov_b32_e32 v233, v137
	global_load_lds_dwordx4 v[234:235], off
	v_lshl_add_u64 v[234:235], s[2:3], 0, v[134:135]
	s_add_i32 m0, s55, 0x2000
	s_nop 0
	global_load_lds_dwordx4 v[234:235], off
	s_mov_b32 m0, s17
	v_lshl_add_u64 v[234:235], s[26:27], 0, v[136:137]
	global_load_lds_dwordx4 v136, s[26:27]
	s_mov_b32 m0, s35
	s_nop 0
	global_load_lds_dwordx4 v232, s[26:27]
	s_waitcnt vmcnt(8)
	s_waitcnt lgkmcnt(0)
	v_lshl_add_u64 v[232:233], s[26:27], 0, v[232:233]
	s_barrier
	s_setprio 1
	s_waitcnt lgkmcnt(0)
	v_mfma_f32_16x16x32_bf16 v[62:65], v[166:169], v[200:203], v[62:65]
	v_mfma_f32_16x16x32_bf16 v[58:61], v[174:177], v[200:203], v[58:61]
	v_mfma_f32_16x16x32_bf16 v[46:49], v[166:169], v[204:207], v[46:49]
	v_mfma_f32_16x16x32_bf16 v[42:45], v[174:177], v[204:207], v[42:45]
	v_mfma_f32_16x16x32_bf16 v[30:33], v[166:169], v[216:219], v[30:33]
	v_mfma_f32_16x16x32_bf16 v[26:29], v[174:177], v[216:219], v[26:29]
	v_mfma_f32_16x16x32_bf16 v[14:17], v[166:169], v[220:223], v[14:17]
	v_mfma_f32_16x16x32_bf16 v[10:13], v[174:177], v[220:223], v[10:13]
	v_mfma_f32_16x16x32_bf16 v[62:65], v[170:173], v[208:211], v[62:65]
	v_mfma_f32_16x16x32_bf16 v[58:61], v[178:181], v[208:211], v[58:61]
	v_mfma_f32_16x16x32_bf16 v[46:49], v[170:173], v[212:215], v[46:49]
	v_mfma_f32_16x16x32_bf16 v[42:45], v[178:181], v[212:215], v[42:45]
	v_mfma_f32_16x16x32_bf16 v[30:33], v[170:173], v[224:227], v[30:33]
	v_mfma_f32_16x16x32_bf16 v[26:29], v[178:181], v[224:227], v[26:29]
	v_mfma_f32_16x16x32_bf16 v[14:17], v[170:173], v[228:231], v[14:17]
	v_mfma_f32_16x16x32_bf16 v[10:13], v[178:181], v[228:231], v[10:13]
	s_setprio 0
	s_setprio 1
	v_mfma_f32_16x16x32_bf16 v[54:57], v[182:185], v[200:203], v[54:57]
	v_mfma_f32_16x16x32_bf16 v[50:53], v[190:193], v[200:203], v[50:53]
	v_mfma_f32_16x16x32_bf16 v[38:41], v[182:185], v[204:207], v[38:41]
	v_mfma_f32_16x16x32_bf16 v[34:37], v[190:193], v[204:207], v[34:37]
	v_mfma_f32_16x16x32_bf16 v[22:25], v[182:185], v[216:219], v[22:25]
	v_mfma_f32_16x16x32_bf16 v[18:21], v[190:193], v[216:219], v[18:21]
	v_mfma_f32_16x16x32_bf16 v[6:9], v[182:185], v[220:223], v[6:9]
	v_mfma_f32_16x16x32_bf16 v[2:5], v[190:193], v[220:223], v[2:5]
	v_mfma_f32_16x16x32_bf16 v[54:57], v[186:189], v[208:211], v[54:57]
	v_mfma_f32_16x16x32_bf16 v[50:53], v[194:197], v[208:211], v[50:53]
	v_mfma_f32_16x16x32_bf16 v[38:41], v[186:189], v[212:215], v[38:41]
	v_mfma_f32_16x16x32_bf16 v[34:37], v[194:197], v[212:215], v[34:37]
	v_mfma_f32_16x16x32_bf16 v[22:25], v[186:189], v[224:227], v[22:25]
	v_mfma_f32_16x16x32_bf16 v[18:21], v[194:197], v[224:227], v[18:21]
	v_mfma_f32_16x16x32_bf16 v[6:9], v[186:189], v[228:231], v[6:9]
	v_mfma_f32_16x16x32_bf16 v[2:5], v[194:197], v[228:231], v[2:5]
	s_setprio 0
	s_barrier
; #define PG8_STAGE(bufoff, gbase, voff) do { _Pragma("unroll") for (int _i = 0; _i < 2; ++_i) \
;         __builtin_amdgcn_global_load_lds((const unsigned*)((const char*)(gbase) + (voff)[_i]), (LAS unsigned*)(lds + (bufoff) + ldsw + _i * 8192), 16, 0, 0); } while (0)
; #define PG8_LDA(dst, b, h) do { _Pragma("unroll") for (int m = 0; m < 4; ++m) _Pragma("unroll") for (int k = 0; k < 2; ++k) dst[m][k] = *(const LAS bf16x8*)(lds + PG8_SA(b, h) + ((aoff ^ (k * 64)) + m * 2048)); } while (0)
; #define PG8_LDB(dst, b, h) do { _Pragma("unroll") for (int n = 0; n < 2; ++n) _Pragma("unroll") for (int k = 0; k < 2; ++k) dst[n][k] = *(const LAS bf16x8*)(lds + PG8_SB(b, h) + ((boff ^ (k * 64)) + n * 2048)); } while (0)
; #define PG8_MMA(ai, bj, At, Bt) do { __builtin_amdgcn_s_setprio(1); _Pragma("unroll") for (int m = 0; m < 4; ++m) _Pragma("unroll") for (int n = 0; n < 2; ++n) _Pragma("unroll") for (int k = 0; k < 2; ++k) \
;         acc[ai][bj][m][n] = __builtin_amdgcn_mfma_f32_16x16x32_bf16(Bt[n][k], At[m][k], acc[ai][bj][m][n], 0, 0, 0); __builtin_amdgcn_s_setprio(0); } while (0)
; #define PG8_WAIT_V(n) asm volatile("s_waitcnt vmcnt(" #n ")" ::: "memory")
; #define PG8_WAIT_L(n) asm volatile("s_waitcnt lgkmcnt(" #n ")" ::: "memory")
; #define PG8_BAR __builtin_amdgcn_s_barrier()
; #define PG8_SCHED __builtin_amdgcn_sched_barrier(0)
;     ...
;             PG8_LDB(B0, 1, 0); PG8_LDB(B1, 1, 1); PG8_SCHED; PG8_LDA(At, 1, 0); PG8_STAGE(PG8_SA(0, 1), a2, vs[1]);
;             PG8_WAIT_V(8); PG8_WAIT_L(0); PG8_BAR; if (do0) { PG8_MMA(0, 0, At, B0); PG8_MMA(0, 1, At, B1); } PG8_BAR; PG8_SCHED;
;             PG8_LDA(At, 1, 1); PG8_STAGE(PG8_SB(1, 0), b3, voffB); PG8_STAGE(PG8_SB(1, 1), b3 + hstep, voffB); PG8_STAGE(PG8_SA(1, 0), a3, vs[0]);
;             PG8_WAIT_V(8); PG8_WAIT_L(0); PG8_BAR; if (do1) { PG8_MMA(1, 0, At, B0); PG8_MMA(1, 1, At, B1); } PG8_BAR; PG8_SCHED;
	s_add_i32 s2, 0, 0x18000
	v_add_u32_e32 v136, s2, v159
	v_add_u32_e32 v151, s2, v160
	ds_read_b128 v[166:169], v136
	ds_read_b128 v[170:173], v151
	v_add_u32_e32 v136, s47, v159
	s_add_i32 s55, 0, 0x1c000
	v_add_u32_e32 v151, s47, v160
	ds_read_b128 v[174:177], v136
	ds_read_b128 v[178:181], v151
	v_add_u32_e32 v136, s55, v159
	v_add_u32_e32 v151, s55, v160
	ds_read_b128 v[182:185], v136
	ds_read_b128 v[186:189], v151
	v_add_u32_e32 v136, s48, v159
	v_add_u32_e32 v151, s48, v160
	ds_read_b128 v[190:193], v136
	ds_read_b128 v[194:197], v151
	s_mov_b32 m0, s36
	ds_read_b128 v[200:203], v161 offset:32768
	ds_read_b128 v[204:207], v161 offset:34816
	ds_read_b128 v[208:211], v162 offset:32768
	ds_read_b128 v[212:215], v162 offset:34816
	ds_read_b128 v[216:219], v161 offset:36864
	ds_read_b128 v[220:223], v161 offset:38912
	ds_read_b128 v[224:227], v162 offset:36864
	ds_read_b128 v[228:231], v162 offset:38912
	global_load_lds_dwordx4 v145, s[26:27]
	s_mov_b32 m0, s37
	s_nop 0
	global_load_lds_dwordx4 v149, s[26:27]
	s_waitcnt vmcnt(8)
	s_waitcnt lgkmcnt(0)
	s_barrier
	s_setprio 1
	s_waitcnt lgkmcnt(0)
	v_mfma_f32_16x16x32_bf16 v[126:129], v[166:169], v[200:203], v[126:129]
	v_mfma_f32_16x16x32_bf16 v[122:125], v[174:177], v[200:203], v[122:125]
	v_mfma_f32_16x16x32_bf16 v[110:113], v[166:169], v[204:207], v[110:113]
	v_mfma_f32_16x16x32_bf16 v[106:109], v[174:177], v[204:207], v[106:109]
	v_mfma_f32_16x16x32_bf16 v[94:97], v[166:169], v[216:219], v[94:97]
	v_mfma_f32_16x16x32_bf16 v[90:93], v[174:177], v[216:219], v[90:93]
	v_mfma_f32_16x16x32_bf16 v[78:81], v[166:169], v[220:223], v[78:81]
	v_mfma_f32_16x16x32_bf16 v[74:77], v[174:177], v[220:223], v[74:77]
	v_mfma_f32_16x16x32_bf16 v[126:129], v[170:173], v[208:211], v[126:129]
	v_mfma_f32_16x16x32_bf16 v[122:125], v[178:181], v[208:211], v[122:125]
	v_mfma_f32_16x16x32_bf16 v[110:113], v[170:173], v[212:215], v[110:113]
	v_mfma_f32_16x16x32_bf16 v[106:109], v[178:181], v[212:215], v[106:109]
	v_mfma_f32_16x16x32_bf16 v[94:97], v[170:173], v[224:227], v[94:97]
	v_mfma_f32_16x16x32_bf16 v[90:93], v[178:181], v[224:227], v[90:93]
	v_mfma_f32_16x16x32_bf16 v[78:81], v[170:173], v[228:231], v[78:81]
	v_mfma_f32_16x16x32_bf16 v[74:77], v[178:181], v[228:231], v[74:77]
	s_setprio 0
	s_setprio 1
	v_mfma_f32_16x16x32_bf16 v[118:121], v[182:185], v[200:203], v[118:121]
	v_mfma_f32_16x16x32_bf16 v[114:117], v[190:193], v[200:203], v[114:117]
	v_mfma_f32_16x16x32_bf16 v[102:105], v[182:185], v[204:207], v[102:105]
	v_mfma_f32_16x16x32_bf16 v[98:101], v[190:193], v[204:207], v[98:101]
	v_mfma_f32_16x16x32_bf16 v[86:89], v[182:185], v[216:219], v[86:89]
	v_mfma_f32_16x16x32_bf16 v[82:85], v[190:193], v[216:219], v[82:85]
	v_mfma_f32_16x16x32_bf16 v[70:73], v[182:185], v[220:223], v[70:73]
	v_mfma_f32_16x16x32_bf16 v[66:69], v[190:193], v[220:223], v[66:69]
	v_mfma_f32_16x16x32_bf16 v[118:121], v[186:189], v[208:211], v[118:121]
	v_mfma_f32_16x16x32_bf16 v[114:117], v[194:197], v[208:211], v[114:117]
	v_mfma_f32_16x16x32_bf16 v[102:105], v[186:189], v[212:215], v[102:105]
	v_mfma_f32_16x16x32_bf16 v[98:101], v[194:197], v[212:215], v[98:101]
	v_mfma_f32_16x16x32_bf16 v[86:89], v[186:189], v[224:227], v[86:89]
	v_mfma_f32_16x16x32_bf16 v[82:85], v[194:197], v[224:227], v[82:85]
	v_mfma_f32_16x16x32_bf16 v[70:73], v[186:189], v[228:231], v[70:73]
	v_mfma_f32_16x16x32_bf16 v[66:69], v[194:197], v[228:231], v[66:69]
	s_setprio 0
	s_barrier
; #define PG8_WAIT_V(n) asm volatile("s_waitcnt vmcnt(" #n ")" ::: "memory")
; #define PG8_WAIT_L(n) asm volatile("s_waitcnt lgkmcnt(" #n ")" ::: "memory")
;     ...
;         for (int t = 0; t < nt; t += 2) {
;             const bool last = (t == nt - 2);
;             const char* a1 = cA + (size_t)(t + 1) * kstepA;
;             const char* a2 = last ? nA : cA + (size_t)(t + 2) * kstepA; const char* b2 = last ? nB : cB + (size_t)(t + 2) * kstepB;
;             const char* a3 = a2 + kstepA; const char* b3 = b2 + kstepB;
;             unsigned vs[2][2];
;             if constexpr (GATHER) {
;                 if (last && has_next) {
; #pragma unroll
;                     for (int hh = 0; hh < 2; ++hh)
; #pragma unroll
;                         for (int i = 0; i < 2; ++i) voffN[hh][i] = (unsigned)idxl[(ui + 1) * 256 + hh * HALF + sR[i]] * (unsigned)(K * 2) + (unsigned)sC[i] * 2u;
;                 }
; #pragma unroll
;                 for (int hh = 0; hh < 2; ++hh)
; #pragma unroll
;                     for (int i = 0; i < 2; ++i) vs[hh][i] = last ? voffN[hh][i] : voffA[hh][i];
;             } else {
; #pragma unroll
;                 for (int hh = 0; hh < 2; ++hh)
; #pragma unroll
;                     for (int i = 0; i < 2; ++i) vs[hh][i] = voffA[hh][i];
;             }
;             PG8_LDB(B0, 0, 0); PG8_LDB(B1, 0, 1); PG8_SCHED; PG8_LDA(At, 0, 0); PG8_STAGE(PG8_SA(1, 1), a1, voffA[1]);
;             PG8_WAIT_V(8); PG8_WAIT_L(0); PG8_BAR; if (do0) { PG8_MMA(0, 0, At, B0); PG8_MMA(0, 1, At, B1); } PG8_BAR; PG8_SCHED;
;             PG8_LDA(At, 0, 1); PG8_STAGE(PG8_SB(0, 0), b2, voffB); PG8_STAGE(PG8_SB(0, 1), b2 + hstep, voffB); PG8_STAGE(PG8_SA(0, 0), a2, vs[0]);
;             PG8_WAIT_V(8); PG8_WAIT_L(0); PG8_BAR; if (do1) { PG8_MMA(1, 0, At, B0); PG8_MMA(1, 1, At, B1); } PG8_BAR; PG8_SCHED;
;             PG8_LDB(B0, 1, 0); PG8_LDB(B1, 1, 1); PG8_SCHED; PG8_LDA(At, 1, 0); PG8_STAGE(PG8_SA(0, 1), a2, vs[1]);
;             PG8_WAIT_V(8); PG8_WAIT_L(0); PG8_BAR; if (do0) { PG8_MMA(0, 0, At, B0); PG8_MMA(0, 1, At, B1); } PG8_BAR; PG8_SCHED;
;             PG8_LDA(At, 1, 1); PG8_STAGE(PG8_SB(1, 0), b3, voffB); PG8_STAGE(PG8_SB(1, 1), b3 + hstep, voffB); PG8_STAGE(PG8_SA(1, 0), a3, vs[0]);
;             PG8_WAIT_V(8); PG8_WAIT_L(0); PG8_BAR; if (do1) { PG8_MMA(1, 0, At, B0); PG8_MMA(1, 1, At, B1); } PG8_BAR; PG8_SCHED;
;         }
	s_add_i32 s2, s2, s34
	v_lshl_add_u64 v[236:237], s[24:25], 0, v[132:133]
	s_mov_b32 m0, s2
	ds_read_b128 v[200:203], v161 offset:49152
	ds_read_b128 v[204:207], v161 offset:51200
	ds_read_b128 v[208:211], v162 offset:49152
	ds_read_b128 v[212:215], v162 offset:51200
	ds_read_b128 v[216:219], v161 offset:53248
	ds_read_b128 v[220:223], v161 offset:55296
	ds_read_b128 v[224:227], v162 offset:53248
	ds_read_b128 v[228:231], v162 offset:55296
	global_load_lds_dwordx4 v[236:237], off
	s_add_i32 m0, s2, 0x2000
	s_add_u32 s2, s22, 0x44000
	v_lshl_add_u64 v[236:237], s[24:25], 0, v[134:135]
	s_addc_u32 s3, s23, 0
	s_add_i32 s22, s55, s34
	global_load_lds_dwordx4 v[236:237], off
	v_lshl_add_u64 v[236:237], s[2:3], 0, v[132:133]
	s_mov_b32 m0, s22
	v_lshl_add_u64 v[234:235], v[234:235], 0, s[10:11]
	global_load_lds_dwordx4 v[236:237], off
	v_lshl_add_u64 v[236:237], s[2:3], 0, v[134:135]
	s_add_i32 m0, s22, 0x2000
	v_lshl_add_u64 v[232:233], v[232:233], 0, s[10:11]
	global_load_lds_dwordx4 v[236:237], off
	s_mov_b32 m0, s41
	s_nop 0
	global_load_lds_dwordx4 v[234:235], off
	s_mov_b32 m0, s42
	s_nop 0
	global_load_lds_dwordx4 v[232:233], off
	s_waitcnt vmcnt(8)
	s_waitcnt lgkmcnt(0)
	s_barrier
	s_setprio 1
	s_waitcnt lgkmcnt(0)
	v_mfma_f32_16x16x32_bf16 v[62:65], v[166:169], v[200:203], v[62:65]
	v_mfma_f32_16x16x32_bf16 v[58:61], v[174:177], v[200:203], v[58:61]
	v_mfma_f32_16x16x32_bf16 v[46:49], v[166:169], v[204:207], v[46:49]
	v_mfma_f32_16x16x32_bf16 v[42:45], v[174:177], v[204:207], v[42:45]
	v_mfma_f32_16x16x32_bf16 v[30:33], v[166:169], v[216:219], v[30:33]
	v_mfma_f32_16x16x32_bf16 v[26:29], v[174:177], v[216:219], v[26:29]
	v_mfma_f32_16x16x32_bf16 v[14:17], v[166:169], v[220:223], v[14:17]
	v_mfma_f32_16x16x32_bf16 v[10:13], v[174:177], v[220:223], v[10:13]
	v_mfma_f32_16x16x32_bf16 v[62:65], v[170:173], v[208:211], v[62:65]
	v_mfma_f32_16x16x32_bf16 v[58:61], v[178:181], v[208:211], v[58:61]
	v_mfma_f32_16x16x32_bf16 v[46:49], v[170:173], v[212:215], v[46:49]
	v_mfma_f32_16x16x32_bf16 v[42:45], v[178:181], v[212:215], v[42:45]
	v_mfma_f32_16x16x32_bf16 v[30:33], v[170:173], v[224:227], v[30:33]
	v_mfma_f32_16x16x32_bf16 v[26:29], v[178:181], v[224:227], v[26:29]
	v_mfma_f32_16x16x32_bf16 v[14:17], v[170:173], v[228:231], v[14:17]
	v_mfma_f32_16x16x32_bf16 v[10:13], v[178:181], v[228:231], v[10:13]
	s_setprio 0
	s_setprio 1
	v_mfma_f32_16x16x32_bf16 v[54:57], v[182:185], v[200:203], v[54:57]
	v_mfma_f32_16x16x32_bf16 v[50:53], v[190:193], v[200:203], v[50:53]
	v_mfma_f32_16x16x32_bf16 v[38:41], v[182:185], v[204:207], v[38:41]
	v_mfma_f32_16x16x32_bf16 v[34:37], v[190:193], v[204:207], v[34:37]
	v_mfma_f32_16x16x32_bf16 v[22:25], v[182:185], v[216:219], v[22:25]
	v_mfma_f32_16x16x32_bf16 v[18:21], v[190:193], v[216:219], v[18:21]
	v_mfma_f32_16x16x32_bf16 v[6:9], v[182:185], v[220:223], v[6:9]
	v_mfma_f32_16x16x32_bf16 v[2:5], v[190:193], v[220:223], v[2:5]
	v_mfma_f32_16x16x32_bf16 v[54:57], v[186:189], v[208:211], v[54:57]
	v_mfma_f32_16x16x32_bf16 v[50:53], v[194:197], v[208:211], v[50:53]
	v_mfma_f32_16x16x32_bf16 v[38:41], v[186:189], v[212:215], v[38:41]
	v_mfma_f32_16x16x32_bf16 v[34:37], v[194:197], v[212:215], v[34:37]
	v_mfma_f32_16x16x32_bf16 v[22:25], v[186:189], v[224:227], v[22:25]
	v_mfma_f32_16x16x32_bf16 v[18:21], v[194:197], v[224:227], v[18:21]
	v_mfma_f32_16x16x32_bf16 v[6:9], v[186:189], v[228:231], v[6:9]
	v_mfma_f32_16x16x32_bf16 v[2:5], v[194:197], v[228:231], v[2:5]
	s_setprio 0
	s_barrier
	s_add_i32 s54, s54, 2
	s_add_u32 s20, s20, 0x100
	s_and_b32 s20, s20, 0x7ff
	s_add_u32 s13, s13, 0x8000
	s_addc_u32 s53, s53, 0
	s_add_u32 s101, s20, 0x100
	s_and_b32 s101, s101, 0x7ff
	s_cmp_eq_u32 s101, 0
	s_cselect_b32 s101, 0x40000, 0
	s_sub_u32 s13, s13, s101
	s_subb_u32 s53, s53, 0
	s_cmp_gt_u32 s54, 13
	s_cbranch_scc1 .LBB0_2340
.LBB0_2338:
	s_cmp_eq_u32 s54, 12
	s_cselect_b64 s[2:3], -1, 0
	s_and_b64 s[22:23], s[18:19], s[2:3]
	s_andn2_b64 vcc, exec, s[22:23]
	s_cbranch_vccnz .LBB0_2337
	ds_read2st64_b32 v[164:165], v143 offset1:2
	ds_read2st64_b32 v[146:147], v141 offset1:2
	s_waitcnt lgkmcnt(0)
	v_lshlrev_b32_e32 v136, 11, v164
	v_lshlrev_b32_e32 v145, 11, v146
	v_lshl_or_b32 v164, v147, 11, v130
	v_or_b32_e32 v147, v136, v1
	v_or_b32_e32 v146, v145, v130
	v_lshl_or_b32 v165, v165, 11, v1
	s_branch .LBB0_2337

; #define LAS __attribute__((address_space(3)))
; __device__ __forceinline__ unsigned xb_ld(unsigned* p)              { return __hip_atomic_load(p, __ATOMIC_RELAXED, __HIP_MEMORY_SCOPE_AGENT); }
; __device__ __forceinline__ unsigned xb_add(unsigned* p, unsigned v) { return __hip_atomic_fetch_add(p, v, __ATOMIC_RELAXED, __HIP_MEMORY_SCOPE_AGENT); }
; __device__ __forceinline__ unsigned xb_xcc_id() { return (unsigned)__builtin_amdgcn_s_getreg((3 << 11) | 20) & 0xFu; }
; __global__ __launch_bounds__(NTHR, 2) void mega(Params p) {
;     extern __shared__ __attribute__((aligned(16))) unsigned char smem[];
;     LAS unsigned char* lds = (LAS unsigned char*)smem;
;     volatile LAS unsigned* st = (volatile LAS unsigned*)(lds + LDS_BYTES - 16);
;     if (threadIdx.x == 0) { st[0] = 0u; st[1] = 0u; st[2] = 0u; st[3] = 0u; }
;     __syncthreads();
;     XcdBarrier bar; bar.bar = WSP(unsigned, OFF_BAR); bar.x = xb_xcc_id(); bar.st = st;
;     if (threadIdx.x == 0) st[2] = xb_add(&bar.bar[XB_XCNT(bar.x)], 1u);
;     run_phase<0>((int)blockIdx.x, p, lds);
;     xcd_barrier(bar);
;     if (threadIdx.x == 0) {
;         bool uni = gridDim.x == 256;
; #pragma unroll
;         for (unsigned j = 0; j < 16; ++j) { const unsigned cnt = xb_ld(&bar.bar[XB_XCNT(j)]); uni = uni && (cnt == (j < 8 ? 32u : 0u)); }
;         st[3] = uni ? st[2] * 8u + bar.x : blockIdx.x;
;     }
;     __syncthreads();
;     const int vc = (int)st[3];
;     run_all<1>(vc, p, lds, bar);
; }
	.amdhsa_kernel _ZN12_GLOBAL__N_14megaENS_6ParamsE
		.amdhsa_group_segment_fixed_size 0
		.amdhsa_private_segment_fixed_size 0
		.amdhsa_kernarg_size 448
		.amdhsa_user_sgpr_count 2
		.amdhsa_user_sgpr_dispatch_ptr 0
		.amdhsa_user_sgpr_queue_ptr 0
		.amdhsa_user_sgpr_kernarg_segment_ptr 1
		.amdhsa_user_sgpr_dispatch_id 0
		.amdhsa_user_sgpr_kernarg_preload_length 0
		.amdhsa_user_sgpr_kernarg_preload_offset 0
		.amdhsa_user_sgpr_private_segment_size 0
		.amdhsa_uses_dynamic_stack 0
		.amdhsa_enable_private_segment 0
		.amdhsa_system_sgpr_workgroup_id_x 1
		.amdhsa_system_sgpr_workgroup_id_y 0
		.amdhsa_system_sgpr_workgroup_id_z 0
		.amdhsa_system_sgpr_workgroup_info 0
		.amdhsa_system_vgpr_workitem_id 0
		.amdhsa_next_free_vgpr 251
		.amdhsa_next_free_sgpr 102
		.amdhsa_accum_offset 252
		.amdhsa_reserve_vcc 1
		.amdhsa_float_round_mode_32 0
		.amdhsa_float_round_mode_16_64 0
		.amdhsa_float_denorm_mode_32 3
		.amdhsa_float_denorm_mode_16_64 3
		.amdhsa_dx10_clamp 1
		.amdhsa_ieee_mode 1
		.amdhsa_fp16_overflow 0
		.amdhsa_tg_split 0
		.amdhsa_exception_fp_ieee_invalid_op 0
		.amdhsa_exception_fp_denorm_src 0
		.amdhsa_exception_fp_ieee_div_zero 0
		.amdhsa_exception_fp_ieee_overflow 0
		.amdhsa_exception_fp_ieee_underflow 0
		.amdhsa_exception_fp_ieee_inexact 0
		.amdhsa_exception_int_div_zero 0
	.end_amdhsa_kernel

; #define LAS __attribute__((address_space(3)))
; __device__ __forceinline__ unsigned xb_ld(unsigned* p)              { return __hip_atomic_load(p, __ATOMIC_RELAXED, __HIP_MEMORY_SCOPE_AGENT); }
; __device__ __forceinline__ unsigned xb_add(unsigned* p, unsigned v) { return __hip_atomic_fetch_add(p, v, __ATOMIC_RELAXED, __HIP_MEMORY_SCOPE_AGENT); }
; __device__ __forceinline__ unsigned xb_xcc_id() { return (unsigned)__builtin_amdgcn_s_getreg((3 << 11) | 20) & 0xFu; }
; __global__ __launch_bounds__(NTHR, 2) void mega(Params p) {
;     extern __shared__ __attribute__((aligned(16))) unsigned char smem[];
;     LAS unsigned char* lds = (LAS unsigned char*)smem;
;     volatile LAS unsigned* st = (volatile LAS unsigned*)(lds + LDS_BYTES - 16);
;     if (threadIdx.x == 0) { st[0] = 0u; st[1] = 0u; st[2] = 0u; st[3] = 0u; }
;     __syncthreads();
;     XcdBarrier bar; bar.bar = WSP(unsigned, OFF_BAR); bar.x = xb_xcc_id(); bar.st = st;
;     if (threadIdx.x == 0) st[2] = xb_add(&bar.bar[XB_XCNT(bar.x)], 1u);
;     run_phase<0>((int)blockIdx.x, p, lds);
;     xcd_barrier(bar);
;     if (threadIdx.x == 0) {
;         bool uni = gridDim.x == 256;
; #pragma unroll
;         for (unsigned j = 0; j < 16; ++j) { const unsigned cnt = xb_ld(&bar.bar[XB_XCNT(j)]); uni = uni && (cnt == (j < 8 ? 32u : 0u)); }
;         st[3] = uni ? st[2] * 8u + bar.x : blockIdx.x;
;     }
;     __syncthreads();
;     const int vc = (int)st[3];
;     run_all<1>(vc, p, lds, bar);
; }
amdhsa.kernels:
  - .agpr_count:     0
    .args:
      - .offset:         0
        .size:           192
        .value_kind:     by_value
      - .offset:         192
        .size:           4
        .value_kind:     hidden_block_count_x
      - .offset:         196
        .size:           4
        .value_kind:     hidden_block_count_y
      - .offset:         200
        .size:           4
        .value_kind:     hidden_block_count_z
      - .offset:         204
        .size:           2
        .value_kind:     hidden_group_size_x
      - .offset:         206
        .size:           2
        .value_kind:     hidden_group_size_y
      - .offset:         208
        .size:           2
        .value_kind:     hidden_group_size_z
      - .offset:         210
        .size:           2
        .value_kind:     hidden_remainder_x
      - .offset:         212
        .size:           2
        .value_kind:     hidden_remainder_y
      - .offset:         214
        .size:           2
        .value_kind:     hidden_remainder_z
      - .offset:         232
        .size:           8
        .value_kind:     hidden_global_offset_x
      - .offset:         240
        .size:           8
        .value_kind:     hidden_global_offset_y
      - .offset:         248
        .size:           8
        .value_kind:     hidden_global_offset_z
      - .offset:         256
        .size:           2
        .value_kind:     hidden_grid_dims
      - .offset:         312
        .size:           4
        .value_kind:     hidden_dynamic_lds_size
    .group_segment_fixed_size: 0
    .kernarg_segment_align: 8
    .kernarg_segment_size: 448
    .language:       OpenCL C
    .language_version:
      - 2
      - 0
    .max_flat_workgroup_size: 512
    .name:           _ZN12_GLOBAL__N_14megaENS_6ParamsE
    .private_segment_fixed_size: 0
    .sgpr_count:     108
    .sgpr_spill_count: 59
    .symbol:         _ZN12_GLOBAL__N_14megaENS_6ParamsE.kd
    .uniform_work_group_size: 1
    .uses_dynamic_stack: false
    .vgpr_count:     251
    .vgpr_spill_count: 0
    .wavefront_size: 64
